# attn loop1: K prefetch distance 2 steps (counted vmcnt(2))
# speedup vs baseline: 1.0278x; 1.0278x over previous
.Lp_top:
	s_lshl_b32 s6, s21, 20
	s_add_u32 s4, s4, s6
	s_addc_u32 s5, s5, 0
	v_lshlrev_b32_e32 v54, 4, v0
	v_mov_b32_e32 v55, v63
	s_lshl_b32 s3, s3, 1
	s_mul_i32 s20, s21, 5
	v_lshl_add_u64 v[4:5], s[4:5], 0, v[54:55]
	s_mov_b64 s[4:5], 0x1000000
	s_add_i32 s20, s20, s3
	v_lshl_add_u64 v[170:171], v[4:5], 0, s[4:5]
	s_and_b32 s22, s20, 31
	s_lshl_b32 s4, s20, 12
	s_lshl_b32 s12, s22, 13
	s_add_i32 s5, s4, 0x1000
	v_lshl_add_u64 v[58:59], v[170:171], 0, s[12:13]
	s_mov_b32 s3, 0x80000
	s_and_b32 s5, s5, 0x1f000
	v_add_co_u32_e32 v16, vcc, s3, v58
	s_lshl_b32 s12, s5, 1
	s_nop 0
	v_addc_co_u32_e32 v17, vcc, 0, v59, vcc
	v_lshl_add_u64 v[56:57], v[170:171], 0, s[12:13]
	global_load_dwordx4 v[4:7], v[58:59], off
	global_load_dwordx4 v[8:11], v[56:57], off
	global_load_dwordx4 v[12:15], v[16:17], off
	v_add_co_u32_e32 v16, vcc, s3, v56
	v_lshrrev_b32_e32 v184, 8, v0
	s_nop 0
	v_addc_co_u32_e32 v17, vcc, 0, v57, vcc
	global_load_dwordx4 v[16:19], v[16:17], off
	v_and_b32_e32 v20, 19, v0
	v_lshlrev_b32_e32 v21, 1, v0
	v_and_b32_e32 v2, 4, v2
	v_and_or_b32 v20, v21, 8, v20
	v_lshlrev_b32_e32 v101, 5, v184
	s_addk_i32 s4, 0x2000
	v_or3_b32 v2, v20, v2, v101
	s_and_b32 s4, s4, 0x1f000
	v_mul_u32_u24_e32 v2, 0x48, v2
	s_lshl_b32 s12, s4, 1
	v_lshlrev_b32_e32 v3, 3, v0
	v_lshlrev_b32_e32 v100, 1, v99
	v_lshlrev_b32_e32 v2, 1, v2
	v_lshl_add_u64 v[60:61], v[170:171], 0, s[12:13]
	v_and_b32_e32 v3, 56, v3
	v_add3_u32 v186, 0, v2, v100
	v_add_co_u32_e32 v2, vcc, s3, v60
	v_lshlrev_b32_e32 v68, 1, v3
	s_nop 0
	v_addc_co_u32_e32 v3, vcc, 0, v61, vcc
	global_load_dwordx4 v[162:165], v[60:61], off
	global_load_dwordx4 v[166:169], v[2:3], off
	v_lshrrev_b32_e32 v82, 3, v0
	v_mul_u32_u24_e32 v22, 0x48, v82
	v_lshlrev_b32_e32 v21, 1, v22
	v_add3_u32 v185, 0, v21, v68
	s_mov_b64 s[24:25], 0x80000
	s_add_i32 s17, s20, 3
	s_add_i32 s18, s20, 4
	v_mov_b32_e32 v62, v63
	v_lshrrev_b32_e32 v55, 6, v0
	v_mov_b32_e32 v83, 0
	v_mov_b32_e32 v84, 0
	v_lshl_add_u64 v[70:71], v[58:59], 0, s[24:25]
	v_lshl_add_u64 v[66:67], v[56:57], 0, s[24:25]
	v_lshl_add_u64 v[64:65], v[60:61], 0, s[24:25]
	s_waitcnt vmcnt(5)
	ds_write_b128 v185, v[4:7]
	s_waitcnt vmcnt(3)
	ds_write_b128 v185, v[12:15] offset:9216
	ds_write_b128 v185, v[8:11] offset:18432
	s_waitcnt vmcnt(2)
	ds_write_b128 v185, v[16:19] offset:27648
	s_waitcnt lgkmcnt(0)
	s_barrier
	ds_read_b128 v[2:5], v186
	ds_read_b128 v[38:41], v186 offset:32
	s_waitcnt lgkmcnt(1)
	v_mfma_f32_32x32x16_f16 v[2:17], v[2:5], v[114:117], 0
	ds_read_b128 v[18:21], v186 offset:9216
	ds_read_b128 v[46:49], v186 offset:9248
	s_waitcnt lgkmcnt(1)
	v_mfma_f32_32x32x16_f16 v[18:33], v[18:21], v[130:133], 0
	v_mfma_f32_32x32x16_f16 v[2:17], v[38:41], v[118:121], v[2:17]
	s_waitcnt lgkmcnt(0)
	v_mfma_f32_32x32x16_f16 v[18:33], v[46:49], v[134:137], v[18:33]
	ds_read_b128 v[38:41], v186 offset:64
	ds_read_b128 v[46:49], v186 offset:96
	s_waitcnt lgkmcnt(1)
	v_mfma_f32_32x32x16_f16 v[2:17], v[38:41], v[122:125], v[2:17]
	ds_read_b128 v[38:41], v186 offset:9280
	ds_read_b128 v[50:53], v186 offset:9312
	s_load_dwordx4 s[4:7], s[0:1], 0x38
	s_load_dwordx2 s[14:15], s[0:1], 0x8
	s_mov_b32 s0, -2
	s_mov_b32 s1, 0x3f800000
	s_waitcnt lgkmcnt(0)
	s_barrier
	v_mfma_f32_32x32x16_f16 v[18:33], v[38:41], v[138:141], v[18:33]
	v_mfma_f32_32x32x16_f16 v[2:17], v[46:49], v[126:129], v[2:17]
	v_mfma_f32_32x32x16_f16 v[18:33], v[50:53], v[142:145], v[18:33]
	s_lshl_b32 s12, s17, 13
	s_and_b32 s12, s12, 0x3e000
	s_add_u32 s28, s12, s3
	s_mov_b32 s29, 0
	v_lshl_add_u64 v[176:177], v[170:171], 0, s[12:13]
	global_load_dwordx4 v[50:53], v[176:177], off
	v_lshl_add_u64 v[176:177], v[170:171], 0, s[28:29]
	global_load_dwordx4 v[94:97], v[176:177], off
	s_nop 7
	s_cmp_eq_u32 s37, 1
	s_cbranch_scc0 .Lf_A
	v_mov_b32_e32 v83, 0xf149f2ca
	v_mov_b32_e32 v84, 0xf149f2ca
	s_branch .Ls_A
.Lf_A:
	s_add_i32 s0, s0, 2
	ds_read_b128 v[102:105], v186 offset:18432
	ds_read_b128 v[106:109], v186 offset:27648
	ds_read_b128 v[110:113], v186 offset:18464
	ds_read_b128 v[86:89], v186 offset:27680
	ds_read_b128 v[90:93], v186 offset:18496
	ds_read_b128 v[172:175], v186 offset:27712
	ds_read_b128 v[72:75], v186 offset:18528
	v_exp_f32_e32 v2, v2
	v_exp_f32_e32 v18, v18
	s_waitcnt lgkmcnt(6)
	v_mfma_f32_32x32x16_f16 v[146:161], v[102:105], v[114:117], 0
	v_exp_f32_e32 v3, v3
	v_exp_f32_e32 v19, v19
	v_exp_f32_e32 v4, v4
	v_exp_f32_e32 v20, v20
	s_waitcnt lgkmcnt(5)
	v_mfma_f32_32x32x16_f16 v[34:49], v[106:109], v[130:133], 0
	v_exp_f32_e32 v5, v5
	v_exp_f32_e32 v21, v21
	v_exp_f32_e32 v6, v6
	v_exp_f32_e32 v22, v22
	s_waitcnt lgkmcnt(4)
	v_mfma_f32_32x32x16_f16 v[146:161], v[110:113], v[118:121], v[146:161]
	v_exp_f32_e32 v7, v7
	v_exp_f32_e32 v23, v23
	v_exp_f32_e32 v8, v8
	v_exp_f32_e32 v24, v24
	s_waitcnt lgkmcnt(3)
	v_mfma_f32_32x32x16_f16 v[34:49], v[86:89], v[134:137], v[34:49]
	v_exp_f32_e32 v9, v9
	v_exp_f32_e32 v25, v25
	s_waitcnt vmcnt(2)
	ds_write_b128 v185, v[162:165]
	ds_write_b128 v185, v[166:169] offset:9216
	ds_read_b128 v[238:241], v186 offset:27744
	s_min_u32 s12, s0, 27
	s_add_i32 s12, s18, s12
	s_lshl_b32 s12, s12, 13
	s_and_b32 s12, s12, 0x3e000
	s_add_u32 s28, s12, s3
	s_mov_b32 s29, 0
	v_lshl_add_u64 v[176:177], v[170:171], 0, s[12:13]
	global_load_dwordx4 v[162:165], v[176:177], off
	v_lshl_add_u64 v[176:177], v[170:171], 0, s[28:29]
	global_load_dwordx4 v[166:169], v[176:177], off
	v_exp_f32_e32 v10, v10
	v_exp_f32_e32 v26, v26
	v_exp_f32_e32 v11, v11
	v_exp_f32_e32 v27, v27
	s_waitcnt lgkmcnt(5)
	v_mfma_f32_32x32x16_f16 v[146:161], v[90:93], v[122:125], v[146:161]
	v_exp_f32_e32 v12, v12
	v_exp_f32_e32 v28, v28
	v_exp_f32_e32 v13, v13
	v_exp_f32_e32 v29, v29
	s_waitcnt lgkmcnt(4)
	v_mfma_f32_32x32x16_f16 v[34:49], v[172:175], v[138:141], v[34:49]
	v_exp_f32_e32 v14, v14
	v_exp_f32_e32 v30, v30
	v_exp_f32_e32 v15, v15
	v_exp_f32_e32 v31, v31
	s_waitcnt lgkmcnt(3)
	v_mfma_f32_32x32x16_f16 v[146:161], v[72:75], v[126:129], v[146:161]
	v_exp_f32_e32 v16, v16
	v_exp_f32_e32 v32, v32
	v_exp_f32_e32 v17, v17
	v_exp_f32_e32 v33, v33
	v_add_f32_e32 v2, v2, v3
	v_add_f32_e32 v4, v4, v5
	v_add_f32_e32 v6, v6, v7
	v_add_f32_e32 v8, v8, v9
	v_add_f32_e32 v10, v10, v11
	v_add_f32_e32 v12, v12, v13
	v_add_f32_e32 v14, v14, v15
	v_add_f32_e32 v16, v16, v17
	v_add_f32_e32 v18, v18, v19
	v_add_f32_e32 v20, v20, v21
	s_waitcnt lgkmcnt(0)
	v_mfma_f32_32x32x16_f16 v[34:49], v[238:241], v[142:145], v[34:49]
	v_add_f32_e32 v22, v22, v23
	v_add_f32_e32 v24, v24, v25
	v_add_f32_e32 v26, v26, v27
	v_add_f32_e32 v28, v28, v29
	v_add_f32_e32 v30, v30, v31
	v_add_f32_e32 v32, v32, v33
	v_add_f32_e32 v2, v2, v4
	v_add_f32_e32 v6, v6, v8
	v_add_f32_e32 v10, v10, v12
	v_add_f32_e32 v14, v14, v16
	v_add_f32_e32 v18, v18, v20
	v_add_f32_e32 v22, v22, v24
	v_add_f32_e32 v26, v26, v28
	v_add_f32_e32 v30, v30, v32
	v_add_f32_e32 v2, v2, v6
	v_add_f32_e32 v10, v10, v14
	v_add_f32_e32 v18, v18, v22
	v_add_f32_e32 v26, v26, v30
	v_add_f32_e32 v2, v2, v10
	v_add_f32_e32 v18, v18, v26
	v_add_f32_e32 v63, v63, v2
	v_add_f32_e32 v62, v62, v18
	s_waitcnt lgkmcnt(0)
	s_barrier
.Lf_B:
	ds_read_b128 v[102:105], v186
	ds_read_b128 v[106:109], v186 offset:9216
	ds_read_b128 v[110:113], v186 offset:32
	ds_read_b128 v[86:89], v186 offset:9248
	ds_read_b128 v[90:93], v186 offset:64
	ds_read_b128 v[172:175], v186 offset:9280
	ds_read_b128 v[72:75], v186 offset:96
	v_exp_f32_e32 v146, v146
	v_exp_f32_e32 v34, v34
	s_waitcnt lgkmcnt(6)
	v_mfma_f32_32x32x16_f16 v[2:17], v[102:105], v[114:117], 0
	v_exp_f32_e32 v147, v147
	v_exp_f32_e32 v35, v35
	v_exp_f32_e32 v148, v148
	v_exp_f32_e32 v36, v36
	s_waitcnt lgkmcnt(5)
	v_mfma_f32_32x32x16_f16 v[18:33], v[106:109], v[130:133], 0
	v_exp_f32_e32 v149, v149
	v_exp_f32_e32 v37, v37
	v_exp_f32_e32 v150, v150
	v_exp_f32_e32 v38, v38
	s_waitcnt lgkmcnt(4)
	v_mfma_f32_32x32x16_f16 v[2:17], v[110:113], v[118:121], v[2:17]
	v_exp_f32_e32 v151, v151
	v_exp_f32_e32 v39, v39
	v_exp_f32_e32 v152, v152
	v_exp_f32_e32 v40, v40
	s_waitcnt lgkmcnt(3)
	v_mfma_f32_32x32x16_f16 v[18:33], v[86:89], v[134:137], v[18:33]
	v_exp_f32_e32 v153, v153
	v_exp_f32_e32 v41, v41
	s_waitcnt vmcnt(2)
	ds_write_b128 v185, v[50:53] offset:18432
	ds_write_b128 v185, v[94:97] offset:27648
	ds_read_b128 v[238:241], v186 offset:9312
	s_min_u32 s12, s0, 26
	s_add_i32 s12, s17, s12
	s_add_i32 s12, s12, 2
	s_lshl_b32 s12, s12, 13
	s_and_b32 s12, s12, 0x3e000
	s_add_u32 s28, s12, s3
	s_mov_b32 s29, 0
	v_lshl_add_u64 v[176:177], v[170:171], 0, s[12:13]
	global_load_dwordx4 v[50:53], v[176:177], off
	v_lshl_add_u64 v[176:177], v[170:171], 0, s[28:29]
	global_load_dwordx4 v[94:97], v[176:177], off
	v_exp_f32_e32 v154, v154
	v_exp_f32_e32 v42, v42
	v_exp_f32_e32 v155, v155
	v_exp_f32_e32 v43, v43
	s_waitcnt lgkmcnt(5)
	v_mfma_f32_32x32x16_f16 v[2:17], v[90:93], v[122:125], v[2:17]
	v_exp_f32_e32 v156, v156
	v_exp_f32_e32 v44, v44
	v_exp_f32_e32 v157, v157
	v_exp_f32_e32 v45, v45
	s_waitcnt lgkmcnt(4)
	v_mfma_f32_32x32x16_f16 v[18:33], v[172:175], v[138:141], v[18:33]
	v_exp_f32_e32 v158, v158
	v_exp_f32_e32 v46, v46
	v_exp_f32_e32 v159, v159
	v_exp_f32_e32 v47, v47
	s_waitcnt lgkmcnt(3)
	v_mfma_f32_32x32x16_f16 v[2:17], v[72:75], v[126:129], v[2:17]
	v_exp_f32_e32 v160, v160
	v_exp_f32_e32 v48, v48
	v_exp_f32_e32 v161, v161
	v_exp_f32_e32 v49, v49
	v_add_f32_e32 v146, v146, v147
	v_add_f32_e32 v148, v148, v149
	v_add_f32_e32 v150, v150, v151
	v_add_f32_e32 v152, v152, v153
	v_add_f32_e32 v154, v154, v155
	v_add_f32_e32 v156, v156, v157
	v_add_f32_e32 v158, v158, v159
	v_add_f32_e32 v160, v160, v161
	v_add_f32_e32 v34, v34, v35
	v_add_f32_e32 v36, v36, v37
	s_waitcnt lgkmcnt(0)
	v_mfma_f32_32x32x16_f16 v[18:33], v[238:241], v[142:145], v[18:33]
	v_add_f32_e32 v38, v38, v39
	v_add_f32_e32 v40, v40, v41
	v_add_f32_e32 v42, v42, v43
	v_add_f32_e32 v44, v44, v45
	v_add_f32_e32 v46, v46, v47
	v_add_f32_e32 v48, v48, v49
	v_add_f32_e32 v146, v146, v148
	v_add_f32_e32 v150, v150, v152
	v_add_f32_e32 v154, v154, v156
	v_add_f32_e32 v158, v158, v160
	v_add_f32_e32 v34, v34, v36
	v_add_f32_e32 v38, v38, v40
	v_add_f32_e32 v42, v42, v44
	v_add_f32_e32 v46, v46, v48
	v_add_f32_e32 v146, v146, v150
	v_add_f32_e32 v154, v154, v158
	v_add_f32_e32 v34, v34, v38
	v_add_f32_e32 v42, v42, v46
	v_add_f32_e32 v146, v146, v154
	v_add_f32_e32 v34, v34, v42
	v_add_f32_e32 v63, v63, v146
	v_add_f32_e32 v62, v62, v34
	s_waitcnt lgkmcnt(0)
	s_barrier
	s_cmp_lt_u32 s0, 30
	s_cbranch_scc1 .Lf_A
	s_branch .Ll1_done
.Ls_A:
	s_add_i32 s0, s0, 2
	ds_read_b128 v[102:105], v186 offset:18432
	ds_read_b128 v[106:109], v186 offset:27648
	ds_read_b128 v[110:113], v186 offset:18464
	ds_read_b128 v[86:89], v186 offset:27680
	ds_read_b128 v[90:93], v186 offset:18496
	ds_read_b128 v[172:175], v186 offset:27712
	ds_read_b128 v[72:75], v186 offset:18528
	v_max3_f32 v76, v2, v3, v4
	v_max3_f32 v77, v18, v19, v20
	v_max3_f32 v76, v76, v5, v6
	v_max3_f32 v77, v77, v21, v22
	v_max3_f32 v76, v76, v7, v8
	v_max3_f32 v77, v77, v23, v24
	v_max3_f32 v76, v76, v9, v10
	v_max3_f32 v77, v77, v25, v26
	v_max3_f32 v76, v76, v11, v12
	v_max3_f32 v77, v77, v27, v28
	v_max3_f32 v76, v76, v13, v14
	v_max3_f32 v77, v77, v29, v30
	v_max3_f32 v76, v76, v15, v16
	v_max3_f32 v77, v77, v31, v32
	v_max_f32_e32 v76, v76, v17
	v_max_f32_e32 v77, v77, v33
	v_max_f32_e32 v85, v84, v76
	v_sub_f32_e32 v76, v84, v85
	v_exp_f32_e32 v76, v76
	v_mov_b32_e32 v84, v85
	v_sub_f32_e32 v2, v2, v85
	v_sub_f32_e32 v3, v3, v85
	v_sub_f32_e32 v4, v4, v85
	v_sub_f32_e32 v5, v5, v85
	v_sub_f32_e32 v6, v6, v85
	v_sub_f32_e32 v7, v7, v85
	v_sub_f32_e32 v8, v8, v85
	v_sub_f32_e32 v9, v9, v85
	v_sub_f32_e32 v10, v10, v85
	v_sub_f32_e32 v11, v11, v85
	v_sub_f32_e32 v12, v12, v85
	v_sub_f32_e32 v13, v13, v85
	v_sub_f32_e32 v14, v14, v85
	v_sub_f32_e32 v15, v15, v85
	v_sub_f32_e32 v16, v16, v85
	v_sub_f32_e32 v17, v17, v85
	v_max_f32_e32 v85, v83, v77
	v_sub_f32_e32 v77, v83, v85
	v_exp_f32_e32 v77, v77
	v_mov_b32_e32 v83, v85
	v_sub_f32_e32 v18, v18, v85
	v_sub_f32_e32 v19, v19, v85
	v_sub_f32_e32 v20, v20, v85
	v_sub_f32_e32 v21, v21, v85
	v_sub_f32_e32 v22, v22, v85
	v_sub_f32_e32 v23, v23, v85
	v_sub_f32_e32 v24, v24, v85
	v_sub_f32_e32 v25, v25, v85
	v_sub_f32_e32 v26, v26, v85
	v_sub_f32_e32 v27, v27, v85
	v_sub_f32_e32 v28, v28, v85
	v_sub_f32_e32 v29, v29, v85
	v_sub_f32_e32 v30, v30, v85
	v_sub_f32_e32 v31, v31, v85
	v_sub_f32_e32 v32, v32, v85
	v_sub_f32_e32 v33, v33, v85
	v_exp_f32_e32 v2, v2
	v_exp_f32_e32 v18, v18
	s_waitcnt lgkmcnt(6)
	v_mfma_f32_32x32x16_f16 v[146:161], v[102:105], v[114:117], 0
	v_exp_f32_e32 v3, v3
	v_exp_f32_e32 v19, v19
	v_exp_f32_e32 v4, v4
	v_exp_f32_e32 v20, v20
	s_waitcnt lgkmcnt(5)
	v_mfma_f32_32x32x16_f16 v[34:49], v[106:109], v[130:133], 0
	v_exp_f32_e32 v5, v5
	v_exp_f32_e32 v21, v21
	v_exp_f32_e32 v6, v6
	v_exp_f32_e32 v22, v22
	s_waitcnt lgkmcnt(4)
	v_mfma_f32_32x32x16_f16 v[146:161], v[110:113], v[118:121], v[146:161]
	v_exp_f32_e32 v7, v7
	v_exp_f32_e32 v23, v23
	v_exp_f32_e32 v8, v8
	v_exp_f32_e32 v24, v24
	s_waitcnt lgkmcnt(3)
	v_mfma_f32_32x32x16_f16 v[34:49], v[86:89], v[134:137], v[34:49]
	v_exp_f32_e32 v9, v9
	v_exp_f32_e32 v25, v25
	s_waitcnt vmcnt(2)
	ds_write_b128 v185, v[162:165]
	ds_write_b128 v185, v[166:169] offset:9216
	ds_read_b128 v[238:241], v186 offset:27744
	s_min_u32 s12, s0, 27
	s_add_i32 s12, s18, s12
	s_lshl_b32 s12, s12, 13
	s_and_b32 s12, s12, 0x3e000
	s_add_u32 s28, s12, s3
	s_mov_b32 s29, 0
	v_lshl_add_u64 v[176:177], v[170:171], 0, s[12:13]
	global_load_dwordx4 v[162:165], v[176:177], off
	v_lshl_add_u64 v[176:177], v[170:171], 0, s[28:29]
	global_load_dwordx4 v[166:169], v[176:177], off
	v_exp_f32_e32 v10, v10
	v_exp_f32_e32 v26, v26
	v_exp_f32_e32 v11, v11
	v_exp_f32_e32 v27, v27
	s_waitcnt lgkmcnt(5)
	v_mfma_f32_32x32x16_f16 v[146:161], v[90:93], v[122:125], v[146:161]
	v_exp_f32_e32 v12, v12
	v_exp_f32_e32 v28, v28
	v_exp_f32_e32 v13, v13
	v_exp_f32_e32 v29, v29
	s_waitcnt lgkmcnt(4)
	v_mfma_f32_32x32x16_f16 v[34:49], v[172:175], v[138:141], v[34:49]
	v_exp_f32_e32 v14, v14
	v_exp_f32_e32 v30, v30
	v_exp_f32_e32 v15, v15
	v_exp_f32_e32 v31, v31
	s_waitcnt lgkmcnt(3)
	v_mfma_f32_32x32x16_f16 v[146:161], v[72:75], v[126:129], v[146:161]
	v_exp_f32_e32 v16, v16
	v_exp_f32_e32 v32, v32
	v_exp_f32_e32 v17, v17
	v_exp_f32_e32 v33, v33
	v_add_f32_e32 v2, v2, v3
	v_add_f32_e32 v4, v4, v5
	v_add_f32_e32 v6, v6, v7
	v_add_f32_e32 v8, v8, v9
	v_add_f32_e32 v10, v10, v11
	v_add_f32_e32 v12, v12, v13
	v_add_f32_e32 v14, v14, v15
	v_add_f32_e32 v16, v16, v17
	v_add_f32_e32 v18, v18, v19
	v_add_f32_e32 v20, v20, v21
	s_waitcnt lgkmcnt(0)
	v_mfma_f32_32x32x16_f16 v[34:49], v[238:241], v[142:145], v[34:49]
	v_add_f32_e32 v22, v22, v23
	v_add_f32_e32 v24, v24, v25
	v_add_f32_e32 v26, v26, v27
	v_add_f32_e32 v28, v28, v29
	v_add_f32_e32 v30, v30, v31
	v_add_f32_e32 v32, v32, v33
	v_add_f32_e32 v2, v2, v4
	v_add_f32_e32 v6, v6, v8
	v_add_f32_e32 v10, v10, v12
	v_add_f32_e32 v14, v14, v16
	v_add_f32_e32 v18, v18, v20
	v_add_f32_e32 v22, v22, v24
	v_add_f32_e32 v26, v26, v28
	v_add_f32_e32 v30, v30, v32
	v_add_f32_e32 v2, v2, v6
	v_add_f32_e32 v10, v10, v14
	v_add_f32_e32 v18, v18, v22
	v_add_f32_e32 v26, v26, v30
	v_add_f32_e32 v2, v2, v10
	v_add_f32_e32 v18, v18, v26
	v_fma_f32 v63, v63, v76, v2
	v_fma_f32 v62, v62, v77, v18
	s_waitcnt lgkmcnt(0)
	s_barrier
.Ls_B:
	ds_read_b128 v[102:105], v186
	ds_read_b128 v[106:109], v186 offset:9216
	ds_read_b128 v[110:113], v186 offset:32
	ds_read_b128 v[86:89], v186 offset:9248
	ds_read_b128 v[90:93], v186 offset:64
	ds_read_b128 v[172:175], v186 offset:9280
	ds_read_b128 v[72:75], v186 offset:96
	v_max3_f32 v76, v146, v147, v148
	v_max3_f32 v77, v34, v35, v36
	v_max3_f32 v76, v76, v149, v150
	v_max3_f32 v77, v77, v37, v38
	v_max3_f32 v76, v76, v151, v152
	v_max3_f32 v77, v77, v39, v40
	v_max3_f32 v76, v76, v153, v154
	v_max3_f32 v77, v77, v41, v42
	v_max3_f32 v76, v76, v155, v156
	v_max3_f32 v77, v77, v43, v44
	v_max3_f32 v76, v76, v157, v158
	v_max3_f32 v77, v77, v45, v46
	v_max3_f32 v76, v76, v159, v160
	v_max3_f32 v77, v77, v47, v48
	v_max_f32_e32 v76, v76, v161
	v_max_f32_e32 v77, v77, v49
	v_max_f32_e32 v85, v84, v76
	v_sub_f32_e32 v76, v84, v85
	v_exp_f32_e32 v76, v76
	v_mov_b32_e32 v84, v85
	v_sub_f32_e32 v146, v146, v85
	v_sub_f32_e32 v147, v147, v85
	v_sub_f32_e32 v148, v148, v85
	v_sub_f32_e32 v149, v149, v85
	v_sub_f32_e32 v150, v150, v85
	v_sub_f32_e32 v151, v151, v85
	v_sub_f32_e32 v152, v152, v85
	v_sub_f32_e32 v153, v153, v85
	v_sub_f32_e32 v154, v154, v85
	v_sub_f32_e32 v155, v155, v85
	v_sub_f32_e32 v156, v156, v85
	v_sub_f32_e32 v157, v157, v85
	v_sub_f32_e32 v158, v158, v85
	v_sub_f32_e32 v159, v159, v85
	v_sub_f32_e32 v160, v160, v85
	v_sub_f32_e32 v161, v161, v85
	v_max_f32_e32 v85, v83, v77
	v_sub_f32_e32 v77, v83, v85
	v_exp_f32_e32 v77, v77
	v_mov_b32_e32 v83, v85
	v_sub_f32_e32 v34, v34, v85
	v_sub_f32_e32 v35, v35, v85
	v_sub_f32_e32 v36, v36, v85
	v_sub_f32_e32 v37, v37, v85
	v_sub_f32_e32 v38, v38, v85
	v_sub_f32_e32 v39, v39, v85
	v_sub_f32_e32 v40, v40, v85
	v_sub_f32_e32 v41, v41, v85
	v_sub_f32_e32 v42, v42, v85
	v_sub_f32_e32 v43, v43, v85
	v_sub_f32_e32 v44, v44, v85
	v_sub_f32_e32 v45, v45, v85
	v_sub_f32_e32 v46, v46, v85
	v_sub_f32_e32 v47, v47, v85
	v_sub_f32_e32 v48, v48, v85
	v_sub_f32_e32 v49, v49, v85
	v_exp_f32_e32 v146, v146
	v_exp_f32_e32 v34, v34
	s_waitcnt lgkmcnt(6)
	v_mfma_f32_32x32x16_f16 v[2:17], v[102:105], v[114:117], 0
	v_exp_f32_e32 v147, v147
	v_exp_f32_e32 v35, v35
	v_exp_f32_e32 v148, v148
	v_exp_f32_e32 v36, v36
	s_waitcnt lgkmcnt(5)
	v_mfma_f32_32x32x16_f16 v[18:33], v[106:109], v[130:133], 0
	v_exp_f32_e32 v149, v149
	v_exp_f32_e32 v37, v37
	v_exp_f32_e32 v150, v150
	v_exp_f32_e32 v38, v38
	s_waitcnt lgkmcnt(4)
	v_mfma_f32_32x32x16_f16 v[2:17], v[110:113], v[118:121], v[2:17]
	v_exp_f32_e32 v151, v151
	v_exp_f32_e32 v39, v39
	v_exp_f32_e32 v152, v152
	v_exp_f32_e32 v40, v40
	s_waitcnt lgkmcnt(3)
	v_mfma_f32_32x32x16_f16 v[18:33], v[86:89], v[134:137], v[18:33]
	v_exp_f32_e32 v153, v153
	v_exp_f32_e32 v41, v41
	s_waitcnt vmcnt(2)
	ds_write_b128 v185, v[50:53] offset:18432
	ds_write_b128 v185, v[94:97] offset:27648
	ds_read_b128 v[238:241], v186 offset:9312
	s_min_u32 s12, s0, 26
	s_add_i32 s12, s17, s12
	s_add_i32 s12, s12, 2
	s_lshl_b32 s12, s12, 13
	s_and_b32 s12, s12, 0x3e000
	s_add_u32 s28, s12, s3
	s_mov_b32 s29, 0
	v_lshl_add_u64 v[176:177], v[170:171], 0, s[12:13]
	global_load_dwordx4 v[50:53], v[176:177], off
	v_lshl_add_u64 v[176:177], v[170:171], 0, s[28:29]
	global_load_dwordx4 v[94:97], v[176:177], off
	v_exp_f32_e32 v154, v154
	v_exp_f32_e32 v42, v42
	v_exp_f32_e32 v155, v155
	v_exp_f32_e32 v43, v43
	s_waitcnt lgkmcnt(5)
	v_mfma_f32_32x32x16_f16 v[2:17], v[90:93], v[122:125], v[2:17]
	v_exp_f32_e32 v156, v156
	v_exp_f32_e32 v44, v44
	v_exp_f32_e32 v157, v157
	v_exp_f32_e32 v45, v45
	s_waitcnt lgkmcnt(4)
	v_mfma_f32_32x32x16_f16 v[18:33], v[172:175], v[138:141], v[18:33]
	v_exp_f32_e32 v158, v158
	v_exp_f32_e32 v46, v46
	v_exp_f32_e32 v159, v159
	v_exp_f32_e32 v47, v47
	s_waitcnt lgkmcnt(3)
	v_mfma_f32_32x32x16_f16 v[2:17], v[72:75], v[126:129], v[2:17]
	v_exp_f32_e32 v160, v160
	v_exp_f32_e32 v48, v48
	v_exp_f32_e32 v161, v161
	v_exp_f32_e32 v49, v49
	v_add_f32_e32 v146, v146, v147
	v_add_f32_e32 v148, v148, v149
	v_add_f32_e32 v150, v150, v151
	v_add_f32_e32 v152, v152, v153
	v_add_f32_e32 v154, v154, v155
	v_add_f32_e32 v156, v156, v157
	v_add_f32_e32 v158, v158, v159
	v_add_f32_e32 v160, v160, v161
	v_add_f32_e32 v34, v34, v35
	v_add_f32_e32 v36, v36, v37
	s_waitcnt lgkmcnt(0)
	v_mfma_f32_32x32x16_f16 v[18:33], v[238:241], v[142:145], v[18:33]
	v_add_f32_e32 v38, v38, v39
	v_add_f32_e32 v40, v40, v41
	v_add_f32_e32 v42, v42, v43
	v_add_f32_e32 v44, v44, v45
	v_add_f32_e32 v46, v46, v47
	v_add_f32_e32 v48, v48, v49
	v_add_f32_e32 v146, v146, v148
	v_add_f32_e32 v150, v150, v152
	v_add_f32_e32 v154, v154, v156
	v_add_f32_e32 v158, v158, v160
	v_add_f32_e32 v34, v34, v36
	v_add_f32_e32 v38, v38, v40
	v_add_f32_e32 v42, v42, v44
	v_add_f32_e32 v46, v46, v48
	v_add_f32_e32 v146, v146, v150
	v_add_f32_e32 v154, v154, v158
	v_add_f32_e32 v34, v34, v38
	v_add_f32_e32 v42, v42, v46
	v_add_f32_e32 v146, v146, v154
	v_add_f32_e32 v34, v34, v42
	v_fma_f32 v63, v63, v76, v146
	v_fma_f32 v62, v62, v77, v34
	s_waitcnt lgkmcnt(0)
	s_barrier
	s_cmp_lt_u32 s0, 30
	s_cbranch_scc1 .Ls_A
